# v52 + PEER gather phases take their first two queue tickets statically from a per-launch wave rank inside the XCD (no start-up atomics), queue tickets offset by 2N
# speedup vs baseline: 1.0132x; 1.0019x over previous
.LBB0_1930:
	s_lshl_b32 s94, s38, 10
	s_waitcnt lgkmcnt(0)
	s_barrier
	v_mbcnt_lo_u32_b32 v90, -1, 0
	v_mbcnt_hi_u32_b32 v90, -1, v90
	s_lshl_b64 s[10:11], s[94:95], 2
	v_readlane_b32 s0, v254, 16
	s_add_u32 s2, s0, s10
	v_readlane_b32 s0, v254, 17
	s_getreg_b32 s20, hwreg(HW_REG_XCC_ID, 0, 4)
	s_addc_u32 s3, s0, s11
	s_and_b32 s16, s20, 7
	v_mov_b32_e32 v0, 0
	v_cmp_eq_u32_e64 s[4:5], 0, v90
	s_cmp_lg_u32 s38, 0
	s_cbranch_scc1 .Lrk_have
	s_lshl_b32 s12, s16, 8
	s_add_i32 s12, s12, 0xc0000
	v_mov_b32_e32 v0, s12
	v_mov_b32_e32 v1, 1
	v_readlane_b32 s12, v255, 33
	s_mov_b64 s[6:7], exec
	s_mov_b64 exec, s[4:5]
	global_atomic_add v1, v0, v1, s[92:93] sc0
	s_mov_b64 exec, s[6:7]
	v_mov_b32_e32 v2, s12
	ds_read_b32 v2, v2
	s_waitcnt vmcnt(0) lgkmcnt(0)
	v_readfirstlane_b32 s32, v1
	v_readfirstlane_b32 s12, v2
	s_lshl_b32 s12, s12, 19
	s_or_b32 s32, s32, s12
.Lrk_have:
	s_and_b32 s26, s32, 0xffff
	s_branch .LBB0_1970
	s_and_saveexec_b64 s[6:7], s[4:5]
	s_cbranch_execz .LBB0_1934
	s_mov_b64 s[12:13], exec
	v_mbcnt_lo_u32_b32 v0, s12, 0
	v_mbcnt_hi_u32_b32 v0, s13, v0
	v_cmp_eq_u32_e32 vcc, 0, v0
	s_and_saveexec_b64 s[8:9], vcc
	s_cbranch_execz .LBB0_1933
	s_lshl_b32 s14, s16, 8
	s_bcnt1_i32_b64 s12, s[12:13]
	v_mov_b32_e32 v1, s14
	v_mov_b32_e32 v2, s12
	global_atomic_add v1, v1, v2, s[2:3] sc0

.LBB0_1977:
	s_add_i32 s18, s17, s16
	s_lshr_b32 s12, s32, 16
	s_sub_i32 s12, s26, s12
	v_mov_b32_e32 v91, s12
	v_readlane_b32 s0, v253, 59
.LBB0_1981:
	s_and_b32 s23, s18, 7
	v_readlane_b32 s1, v254, 6
	s_add_u32 s18, s1, s8
	v_readlane_b32 s1, v254, 7
	s_addc_u32 s19, s1, s9
	s_lshl_b32 s6, s26, 3
	v_mov_b32_e32 v8, v90
	s_and_b32 s12, s6, 0x3ff8
	s_lshl_b32 s6, s12, 9
	v_lshlrev_b32_e32 v0, 1, v8
	s_add_u32 s6, s82, s6
	v_ashrrev_i32_e32 v1, 31, v0
	s_addc_u32 s7, s83, 0
	v_lshlrev_b64 v[2:3], 2, v[0:1]
	v_lshl_add_u64 v[4:5], s[6:7], 0, v[2:3]
	s_lshl_b32 s6, s12, 11
	s_add_u32 s6, s85, s6
	s_addc_u32 s7, s0, 0
	s_lshr_b32 s14, s26, 4
	s_lshl_b32 s13, s23, 8
	s_and_b32 s14, s14, 0x80
	s_or_b32 s13, s14, s13
	s_add_u32 s6, s6, s13
	s_addc_u32 s7, s7, 0
	v_lshl_add_u64 v[6:7], s[6:7], 0, v[0:1]
	global_load_dwordx2 v[4:5], v[4:5], off
	s_nop 0
	global_load_ushort v6, v[6:7], off
	s_or_b32 s12, s12, 1
	s_lshl_b32 s6, s12, 9
	s_add_u32 s6, s82, s6
	s_addc_u32 s7, s83, 0
	v_lshl_add_u64 v[2:3], s[6:7], 0, v[2:3]
	s_lshl_b32 s6, s12, 11
	s_add_u32 s6, s85, s6
	s_addc_u32 s7, s0, 0
	s_add_u32 s6, s6, s13
	s_addc_u32 s7, s7, 0
	v_lshl_add_u64 v[0:1], s[6:7], 0, v[0:1]
	global_load_dwordx2 v[88:89], v[2:3], off
	global_load_ushort v92, v[0:1], off
	v_lshlrev_b32_e32 v1, 3, v8
	v_lshlrev_b32_e32 v2, 4, v8
	v_add_u32_e32 v0, s84, v1
	v_and_b32_e32 v1, 0xffffffc0, v1
	v_and_b32_e32 v7, 0x70, v2
	v_mad_u64_u32 v[2:3], s[6:7], v8, -6, v[0:1]
	v_add_u32_e32 v1, s84, v1
	v_add_u32_e32 v16, s84, v7
	s_add_i32 s20, s20, 1
	s_mov_b32 s21, 0
	s_mov_b32 s22, 0
	s_waitcnt vmcnt(3)
	ds_write_b64 v0, v[4:5]
	s_waitcnt vmcnt(2)
	ds_write_b16 v2, v6 offset:512
	s_waitcnt lgkmcnt(0)
	ds_read_b128 v[12:15], v1
	ds_read_b128 v[8:11], v1 offset:16
	ds_read_b128 v[4:7], v1 offset:32
	ds_read_b128 v[0:3], v1 offset:48
	ds_read_b128 v[16:19], v16 offset:512
	s_waitcnt lgkmcnt(0)
.LBB0_1982:
	v_readfirstlane_b32 s24, v91
	s_lshr_b32 s6, s32, 15
	s_add_i32 s24, s24, s6
	s_cmpk_lt_u32 s24, 0x1000
	s_cbranch_scc1 .LBB0_1989
	s_add_i32 s6, s20, s17
	s_lshl_b32 s14, s6, 6
	s_branch .LBB0_1986

.LBB0_2110:
	s_add_u32 s2, s92, s10
	s_waitcnt lgkmcnt(0)
	s_barrier
	v_mbcnt_lo_u32_b32 v94, -1, 0
	v_mbcnt_hi_u32_b32 v94, -1, v94
	s_addc_u32 s3, s93, s11
	s_add_u32 s2, s2, 0x8800
	s_getreg_b32 s18, hwreg(HW_REG_XCC_ID, 0, 4)
	s_addc_u32 s3, s3, 0
	s_and_b32 s14, s18, 7
	v_mov_b32_e32 v0, 0
	v_cmp_eq_u32_e64 s[4:5], 0, v94
	s_and_b32 s23, s32, 0xffff
	s_branch .LBB0_2150
	s_and_saveexec_b64 s[6:7], s[4:5]
	s_cbranch_execz .LBB0_2114
	s_mov_b64 s[12:13], exec
	v_mbcnt_lo_u32_b32 v0, s12, 0
	v_mbcnt_hi_u32_b32 v0, s13, v0
	v_cmp_eq_u32_e32 vcc, 0, v0
	s_and_saveexec_b64 s[10:11], vcc
	s_cbranch_execz .LBB0_2113
	s_lshl_b32 s15, s14, 8
	s_bcnt1_i32_b64 s12, s[12:13]
	v_mov_b32_e32 v1, s15
	v_mov_b32_e32 v2, s12
	global_atomic_add v1, v1, v2, s[2:3] sc0

.LBB0_2157:
	s_add_i32 s16, s15, s14
	s_lshr_b32 s10, s32, 16
	s_sub_i32 s10, s23, s10
	v_mov_b32_e32 v95, s10
.LBB0_2161:
	s_and_b32 s12, s16, 7
	v_readlane_b32 s0, v254, 12
	s_add_u32 s16, s0, s8
	v_readlane_b32 s0, v254, 13
	s_addc_u32 s17, s0, s9
	s_lshl_b32 s6, s23, 10
	v_mov_b32_e32 v8, v94
	s_and_b32 s8, s6, 0x1ffc00
	s_lshl_b32 s6, s8, 2
	v_lshlrev_b32_e32 v0, 1, v8
	s_add_u32 s6, s82, s6
	v_ashrrev_i32_e32 v1, 31, v0
	s_addc_u32 s7, s83, 0
	v_lshlrev_b64 v[2:3], 2, v[0:1]
	v_lshl_add_u64 v[4:5], s[6:7], 0, v[2:3]
	s_add_u32 s6, s56, s8
	s_addc_u32 s7, s57, 0
	v_lshl_add_u64 v[6:7], s[6:7], 0, v[0:1]
	global_load_dwordx2 v[4:5], v[4:5], off
	s_nop 0
	global_load_ushort v6, v[6:7], off
	s_or_b32 s94, s8, 0x80
	v_lshl_add_u64 v[2:3], s[82:83], 0, v[2:3]
	s_lshl_b32 s6, s94, 2
	s_mov_b32 s7, s95
	v_lshl_add_u64 v[2:3], v[2:3], 0, s[6:7]
	v_lshl_add_u64 v[0:1], s[56:57], 0, v[0:1]
	v_lshl_add_u64 v[0:1], v[0:1], 0, s[94:95]
	global_load_dwordx2 v[88:89], v[2:3], off
	global_load_ushort v96, v[0:1], off
	v_ashrrev_i32_e32 v1, 3, v8
	v_lshl_add_u32 v0, v8, 3, s84
	v_mad_u64_u32 v[2:3], s[6:7], v8, -6, v[0:1]
	v_lshl_add_u32 v3, v1, 6, s84
	s_waitcnt vmcnt(20)
	v_lshl_add_u32 v16, v1, 4, s84
	s_add_i32 s18, s18, 1
	s_mov_b32 s19, 0
	s_mov_b32 s20, 0
	s_waitcnt vmcnt(3)
	ds_write_b64 v0, v[4:5]
	s_waitcnt vmcnt(2)
	ds_write_b16 v2, v6 offset:512
	s_waitcnt lgkmcnt(0)
	ds_read_b128 v[12:15], v3
	ds_read_b128 v[8:11], v3 offset:16
	ds_read_b128 v[4:7], v3 offset:32
	ds_read_b128 v[0:3], v3 offset:48
	ds_read_b128 v[16:19], v16 offset:512
	s_waitcnt lgkmcnt(0)
	s_branch .LBB0_2163

.LBB0_2163:
	v_readfirstlane_b32 s13, v95
	s_lshr_b32 s6, s32, 15
	s_add_i32 s13, s13, s6
	s_cmpk_lt_u32 s13, 0x1000
	s_cbranch_scc1 .LBB0_2170
	s_add_i32 s6, s18, s15
	s_lshl_b32 s10, s6, 6
	s_branch .LBB0_2167
